# static s_setprio 1 for waves 4-7 ahead of the topic loop (64-byte block keeps loop placement)
# baseline (speedup 1.0000x reference)
.LBB1_53:
	s_or_b64 exec, exec, s[2:3]
	v_readfirstlane_b32 s74, v0
	s_nop 3
	s_lshr_b32 s74, s74, 6
	s_cmp_ge_u32 s74, 4
	s_cbranch_scc0 .Lnoprio_t
	s_setprio 1
.Lnoprio_t:
	s_nop 0
	s_nop 0
	s_nop 0
	s_nop 0
	s_nop 0
	s_nop 0
	s_nop 0
	s_nop 0
	s_nop 0
	s_nop 0
	v_add_f32_e32 v130, v130, v14
	v_or_b32_e32 v14, v212, v214
	v_add_f32_e32 v134, v134, v10
	v_add_f32_e32 v10, v110, v50
	v_add_f32_e32 v50, v98, v58
	v_add_f32_e32 v58, v90, v62
	v_add_u32_e32 v62, 0x17080, v14
	v_add_f32_e32 v131, v131, v15
	v_add_f32_e32 v132, v132, v16
	v_add_f32_e32 v133, v133, v17
	v_add_f32_e32 v82, v82, v30
	ds_read_b128 v[14:17], v62
	v_add_f32_e32 v83, v83, v31
	v_add_f32_e32 v84, v84, v32
	v_add_f32_e32 v85, v85, v33
	ds_read_b128 v[30:33], v62 offset:32
	v_add_f32_e32 v2, v142, v2
	v_add_f32_e32 v138, v138, v6
	v_add_f32_e32 v6, v126, v34
	v_add_f32_e32 v34, v122, v38
	v_add_f32_e32 v38, v118, v42
	v_add_f32_e32 v114, v114, v46
	v_add_f32_e32 v42, v106, v54
	v_add_f32_e32 v18, v102, v18
	v_add_f32_e32 v46, v94, v22
	v_add_f32_e32 v141, v141, v9
	v_add_f32_e32 v135, v135, v11
	v_add_f32_e32 v136, v136, v12
	v_add_f32_e32 v137, v137, v13
	v_add_f32_e32 v9, v129, v37
	v_add_f32_e32 v37, v125, v41
	v_add_f32_e32 v41, v121, v45
	v_add_f32_e32 v115, v115, v47
	v_add_f32_e32 v116, v116, v48
	v_add_f32_e32 v117, v117, v49
	v_add_f32_e32 v11, v111, v51
	v_add_f32_e32 v12, v112, v52
	v_add_f32_e32 v13, v113, v53
	v_add_f32_e32 v45, v109, v57
	v_add_f32_e32 v51, v99, v59
	v_add_f32_e32 v52, v100, v60
	v_add_f32_e32 v53, v101, v61
	v_add_f32_e32 v59, v91, v63
	v_add_f32_e32 v60, v92, v64
	v_add_f32_e32 v61, v93, v65
	v_add_f32_e32 v57, v86, v26
	s_waitcnt lgkmcnt(1)
	v_add_f32_e32 v2, v14, v2
	v_add_f32_e32 v6, v14, v6
	v_add_f32_e32 v10, v14, v10
	v_add_f32_e32 v14, v14, v18
	s_waitcnt lgkmcnt(0)
	v_add_f32_e32 v18, v30, v138
	v_add_f32_e32 v22, v30, v34
	v_add_f32_e32 v26, v30, v42
	v_add_f32_e32 v30, v30, v46
	ds_read_b128 v[46:49], v62 offset:64
	ds_read_b128 v[62:65], v62 offset:96
	v_add_f32_e32 v3, v143, v3
	v_add_f32_e32 v4, v144, v4
	v_add_f32_e32 v5, v145, v5
	v_add_f32_e32 v139, v139, v7
	v_add_f32_e32 v140, v140, v8
	v_add_f32_e32 v7, v127, v35
	v_add_f32_e32 v8, v128, v36
	v_add_f32_e32 v35, v123, v39
	v_add_f32_e32 v36, v124, v40
	v_add_f32_e32 v39, v119, v43
	v_add_f32_e32 v40, v120, v44
	v_add_f32_e32 v43, v107, v55
	v_add_f32_e32 v44, v108, v56
	v_add_f32_e32 v19, v103, v19
	v_add_f32_e32 v20, v104, v20
	v_add_f32_e32 v21, v105, v21
	v_add_f32_e32 v54, v95, v23
	v_add_f32_e32 v55, v96, v24
	v_add_f32_e32 v56, v97, v25
	v_add_f32_e32 v86, v87, v27
	v_add_f32_e32 v87, v88, v28
	v_add_f32_e32 v88, v89, v29
	v_add_f32_e32 v3, v15, v3
	v_add_f32_e32 v4, v16, v4
	v_add_f32_e32 v5, v17, v5
	v_add_f32_e32 v7, v15, v7
	v_add_f32_e32 v8, v16, v8
	v_add_f32_e32 v9, v17, v9
	v_add_f32_e32 v11, v15, v11
	v_add_f32_e32 v12, v16, v12
	v_add_f32_e32 v13, v17, v13
	v_add_f32_e32 v15, v15, v19
	v_add_f32_e32 v16, v16, v20
	v_add_f32_e32 v17, v17, v21
	v_add_f32_e32 v19, v31, v139
	v_add_f32_e32 v20, v32, v140
	v_add_f32_e32 v21, v33, v141
	v_add_f32_e32 v23, v31, v35
	v_add_f32_e32 v24, v32, v36
	v_add_f32_e32 v25, v33, v37
	v_add_f32_e32 v27, v31, v43
	v_add_f32_e32 v28, v32, v44
	v_add_f32_e32 v29, v33, v45
	v_add_f32_e32 v31, v31, v54
	v_add_f32_e32 v32, v32, v55
	v_add_f32_e32 v33, v33, v56
	s_waitcnt lgkmcnt(1)
	v_add_f32_e32 v34, v46, v134
	v_add_f32_e32 v38, v46, v38
	v_add_f32_e32 v42, v46, v50
	v_add_f32_e32 v43, v47, v51
	v_add_f32_e32 v44, v48, v52
	v_add_f32_e32 v45, v49, v53
	v_add_f32_e32 v46, v46, v57
	s_waitcnt lgkmcnt(0)
	v_add_f32_e32 v50, v62, v130
	v_add_f32_e32 v51, v63, v131
	v_add_f32_e32 v52, v64, v132
	v_add_f32_e32 v53, v65, v133
	v_add_f32_e32 v54, v62, v114
	v_add_f32_e32 v55, v63, v115
	v_add_f32_e32 v56, v64, v116
	v_add_f32_e32 v57, v65, v117
	v_add_f32_e32 v58, v62, v58
	v_add_f32_e32 v59, v63, v59
	v_add_f32_e32 v60, v64, v60
	v_add_f32_e32 v61, v65, v61
	v_add_f32_e32 v62, v62, v82
	v_add_f32_e32 v63, v63, v83
	v_add_f32_e32 v64, v64, v84
	v_add_f32_e32 v65, v65, v85
	s_waitcnt vmcnt(3)
	v_fma_f32 v82, v66, v2, 0
	v_fma_f32 v83, v66, v6, 0
	v_fma_f32 v84, v66, v10, 0
	v_fma_f32 v85, v66, v14, 0
	v_fmac_f32_e32 v82, v67, v3
	v_fmac_f32_e32 v83, v67, v7
	v_fmac_f32_e32 v84, v67, v11
	v_fmac_f32_e32 v85, v67, v15
	v_fmac_f32_e32 v82, v68, v4
	v_fmac_f32_e32 v83, v68, v8
	v_fmac_f32_e32 v84, v68, v12
	v_fmac_f32_e32 v85, v68, v16
	v_fmac_f32_e32 v82, v69, v5
	v_fmac_f32_e32 v83, v69, v9
	v_fmac_f32_e32 v84, v69, v13
	v_fmac_f32_e32 v85, v69, v17
	s_waitcnt vmcnt(2)
	v_fmac_f32_e32 v82, v70, v18
	v_fmac_f32_e32 v83, v70, v22
	v_fmac_f32_e32 v84, v70, v26
	v_fmac_f32_e32 v85, v70, v30
	v_fmac_f32_e32 v82, v71, v19
	v_fmac_f32_e32 v83, v71, v23
	v_fmac_f32_e32 v84, v71, v27
	v_fmac_f32_e32 v85, v71, v31
	v_fmac_f32_e32 v82, v72, v20
	v_fmac_f32_e32 v83, v72, v24
	v_fmac_f32_e32 v84, v72, v28
	v_fmac_f32_e32 v85, v72, v32
	v_fmac_f32_e32 v82, v73, v21
	v_fmac_f32_e32 v83, v73, v25
	v_fmac_f32_e32 v84, v73, v29
	v_fmac_f32_e32 v85, v73, v33
	v_add_f32_e32 v35, v47, v135
	v_add_f32_e32 v39, v47, v39
	v_add_f32_e32 v47, v47, v86
	s_waitcnt vmcnt(1)
	v_fmac_f32_e32 v82, v74, v34
	v_fmac_f32_e32 v83, v74, v38
	v_fmac_f32_e32 v84, v74, v42
	v_fmac_f32_e32 v85, v74, v46
	v_add_f32_e32 v36, v48, v136
	v_add_f32_e32 v40, v48, v40
	v_add_f32_e32 v48, v48, v87
	v_fmac_f32_e32 v82, v75, v35
	v_fmac_f32_e32 v83, v75, v39
	v_fmac_f32_e32 v84, v75, v43
	v_fmac_f32_e32 v85, v75, v47
	v_add_f32_e32 v37, v49, v137
	v_add_f32_e32 v41, v49, v41
	v_add_f32_e32 v49, v49, v88
	v_fmac_f32_e32 v82, v76, v36
	v_fmac_f32_e32 v83, v76, v40
	v_fmac_f32_e32 v84, v76, v44
	v_fmac_f32_e32 v85, v76, v48
	v_fmac_f32_e32 v82, v77, v37
	v_fmac_f32_e32 v83, v77, v41
	v_fmac_f32_e32 v84, v77, v45
	v_fmac_f32_e32 v85, v77, v49
	s_waitcnt vmcnt(0)
	v_fmac_f32_e32 v82, v78, v50
	v_fmac_f32_e32 v83, v78, v54
	v_fmac_f32_e32 v84, v78, v58
	v_fmac_f32_e32 v85, v78, v62
	v_mul_u32_u24_e32 v87, 10, v225
	v_lshlrev_b32_e32 v1, 9, v1
	v_fmac_f32_e32 v82, v79, v51
	v_fmac_f32_e32 v83, v79, v55
	v_fmac_f32_e32 v84, v79, v59
	v_fmac_f32_e32 v85, v79, v63
	v_lshlrev_b32_e32 v86, 9, v87
	v_lshl_or_b32 v1, v87, 12, v1
	v_lshlrev_b32_e32 v87, 10, v224
	v_fmac_f32_e32 v82, v80, v52
	v_fmac_f32_e32 v83, v80, v56
	v_fmac_f32_e32 v84, v80, v60
	v_fmac_f32_e32 v85, v80, v64
	v_or3_b32 v1, v87, v1, v211
	v_fmac_f32_e32 v82, v81, v53
	v_fmac_f32_e32 v83, v81, v57
	v_fmac_f32_e32 v84, v81, v61
	v_fmac_f32_e32 v85, v81, v65
	v_or3_b32 v86, v86, v212, v214
	v_add_u32_e32 v1, 0x2800, v1
	s_mov_b32 s0, 0
	v_mul_f32_e32 v66, 0.5, v66
	v_mul_f32_e32 v67, 0.5, v67
	v_mul_f32_e32 v68, 0.5, v68
	v_mul_f32_e32 v69, 0.5, v69
	v_mul_f32_e32 v70, 0.5, v70
	v_mul_f32_e32 v71, 0.5, v71
	v_mul_f32_e32 v72, 0.5, v72
	v_mul_f32_e32 v73, 0.5, v73
	v_mul_f32_e32 v74, 0.5, v74
	v_mul_f32_e32 v75, 0.5, v75
	v_mul_f32_e32 v76, 0.5, v76
	v_mul_f32_e32 v77, 0.5, v77
	v_mul_f32_e32 v78, 0.5, v78
	v_mul_f32_e32 v79, 0.5, v79
	v_mul_f32_e32 v80, 0.5, v80
	v_mul_f32_e32 v81, 0.5, v81
	v_mul_f32_e32 v82, 0.5, v82
	v_mul_f32_e32 v83, 0.5, v83
	v_mul_f32_e32 v84, 0.5, v84
	v_mul_f32_e32 v85, 0.5, v85
	v_add_u32_e32 v152, s0, v86
	ds_read_b128 v[88:91], v152
	ds_read_b128 v[92:95], v152 offset:32
	ds_read_b128 v[96:99], v152 offset:64
	ds_read_b128 v[100:103], v152 offset:96
	s_addk_i32 s0, 0x200
